# grid barrier: last XCD leader releases every XCD XGEN word directly (no TOPGEN hop); other leaders wait on XGEN like members
# speedup vs baseline: 1.0126x; 1.0126x over previous
.LBB0_190:
	v_readlane_b32 s4, v254, 43
	s_lshl_b32 s4, s4, 8
	v_readlane_b32 s6, v254, 40
	v_readlane_b32 s7, v254, 41
	s_add_u32 s4, s6, s4
	s_addc_u32 s5, s7, 0
	v_mov_b32_e32 v2, 0x1000
	v_mov_b32_e32 v4, 1
	global_atomic_add v4, v2, v4, s[4:5] offset:1024 sc0
	v_cvt_f32_u32_e32 v2, v3
	v_sub_u32_e32 v5, 0, v3
	v_rcp_iflag_f32_e32 v2, v2
	s_nop 0
	v_mul_f32_e32 v2, 0x4f7ffffe, v2
	v_cvt_u32_f32_e32 v2, v2
	v_mul_lo_u32 v5, v5, v2
	v_mul_hi_u32 v5, v2, v5
	v_add_u32_e32 v2, v2, v5
	s_waitcnt vmcnt(0)
	v_mul_hi_u32 v2, v4, v2
	v_mul_lo_u32 v5, v2, v3
	v_sub_u32_e32 v5, v4, v5
	v_add_u32_e32 v6, 1, v2
	v_cmp_ge_u32_e32 vcc, v5, v3
	v_add_u32_e32 v4, 1, v4
	s_nop 0
	v_cndmask_b32_e32 v2, v2, v6, vcc
	v_sub_u32_e32 v6, v5, v3
	v_cndmask_b32_e32 v5, v5, v6, vcc
	v_add_u32_e32 v6, 1, v2
	v_cmp_ge_u32_e32 vcc, v5, v3
	s_nop 1
	v_cndmask_b32_e32 v2, v2, v6, vcc
	v_mul_lo_u32 v5, v3, v2
	v_add_u32_e32 v3, v5, v3
	v_cmp_ne_u32_e32 vcc, v4, v3
	s_cbranch_vccz .Lxb0_lead
.Lxb0_poll:
	s_mov_b32 s10, 0
	v_mov_b32_e32 v4, 0x2000
.Lxb0_spin:
	global_load_dword v5, v4, s[4:5] offset:1024 sc1
	s_waitcnt vmcnt(0)
	v_cmp_ne_u32_e32 vcc, v5, v2
	s_cbranch_vccnz .Lxb0_acq
	s_sleep 1
	s_add_u32 s10, s10, 1
	s_cmp_lt_u32 s10, 0x10000
	s_cbranch_scc1 .Lxb0_spin
	s_branch .Lxb0_acq
.Lxb0_lead:
	buffer_wbl2 sc1
	s_waitcnt vmcnt(0) lgkmcnt(0)
	v_mov_b32_e32 v4, 0x7000
	v_mov_b32_e32 v5, 1
	global_atomic_add v5, v4, v5, s[96:97] offset:1024 sc0
	v_cvt_f32_u32_e32 v4, v1
	v_sub_u32_e32 v6, 0, v1
	v_rcp_iflag_f32_e32 v4, v4
	s_nop 1
	v_mul_f32_e32 v4, 0x4f7ffffe, v4
	v_cvt_u32_f32_e32 v4, v4
	v_mul_lo_u32 v6, v6, v4
	v_mul_hi_u32 v6, v4, v6
	v_add_u32_e32 v4, v4, v6
	s_waitcnt vmcnt(0)
	v_mul_hi_u32 v4, v5, v4
	v_mul_lo_u32 v4, v4, v1
	v_sub_u32_e32 v4, v5, v4
	v_sub_u32_e32 v6, v4, v1
	v_min_u32_e32 v4, v4, v6
	v_sub_u32_e32 v6, v4, v1
	v_min_u32_e32 v4, v4, v6
	v_add_u32_e32 v4, 1, v4
	v_cmp_ne_u32_e32 vcc, v4, v1
	s_cbranch_vccnz .Lxb0_poll
	v_readlane_b32 s8, v254, 40
	v_readlane_b32 s9, v254, 41
	v_mov_b32_e32 v4, 0x2400
	v_mov_b32_e32 v5, 1
	s_nop 3
	global_atomic_add v4, v5, s[8:9]
	global_atomic_add v4, v5, s[8:9] offset:256
	global_atomic_add v4, v5, s[8:9] offset:512
	global_atomic_add v4, v5, s[8:9] offset:768
	global_atomic_add v4, v5, s[8:9] offset:1024
	global_atomic_add v4, v5, s[8:9] offset:1280
	global_atomic_add v4, v5, s[8:9] offset:1536
	global_atomic_add v4, v5, s[8:9] offset:1792
	global_atomic_add v4, v5, s[8:9] offset:2048
	global_atomic_add v4, v5, s[8:9] offset:2304
	global_atomic_add v4, v5, s[8:9] offset:2560
	global_atomic_add v4, v5, s[8:9] offset:2816
	global_atomic_add v4, v5, s[8:9] offset:3072
	global_atomic_add v4, v5, s[8:9] offset:3328
	global_atomic_add v4, v5, s[8:9] offset:3584
	global_atomic_add v4, v5, s[8:9] offset:3840
.Lxb0_acq:
	buffer_inv sc1
	s_waitcnt vmcnt(0)

.LBB0_248:
	v_readlane_b32 s2, v254, 43
	s_lshl_b32 s2, s2, 8
	v_readlane_b32 s4, v254, 40
	v_readlane_b32 s5, v254, 41
	s_add_u32 s2, s4, s2
	s_addc_u32 s3, s5, 0
	v_mov_b32_e32 v2, 0x1000
	v_mov_b32_e32 v4, 1
	global_atomic_add v4, v2, v4, s[2:3] offset:1024 sc0
	v_cvt_f32_u32_e32 v2, v3
	v_sub_u32_e32 v5, 0, v3
	v_rcp_iflag_f32_e32 v2, v2
	s_nop 0
	v_mul_f32_e32 v2, 0x4f7ffffe, v2
	v_cvt_u32_f32_e32 v2, v2
	v_mul_lo_u32 v5, v5, v2
	v_mul_hi_u32 v5, v2, v5
	v_add_u32_e32 v2, v2, v5
	s_waitcnt vmcnt(0)
	v_mul_hi_u32 v2, v4, v2
	v_mul_lo_u32 v5, v2, v3
	v_sub_u32_e32 v5, v4, v5
	v_add_u32_e32 v6, 1, v2
	v_cmp_ge_u32_e32 vcc, v5, v3
	v_add_u32_e32 v4, 1, v4
	s_nop 0
	v_cndmask_b32_e32 v2, v2, v6, vcc
	v_sub_u32_e32 v6, v5, v3
	v_cndmask_b32_e32 v5, v5, v6, vcc
	v_add_u32_e32 v6, 1, v2
	v_cmp_ge_u32_e32 vcc, v5, v3
	s_nop 1
	v_cndmask_b32_e32 v2, v2, v6, vcc
	v_mul_lo_u32 v5, v3, v2
	v_add_u32_e32 v3, v5, v3
	v_cmp_ne_u32_e32 vcc, v4, v3
	s_cbranch_vccz .Lxb1_lead

.Lxb1_spin:
	global_load_dword v5, v4, s[2:3] offset:1024 sc1
	s_waitcnt vmcnt(0)
	v_cmp_ne_u32_e32 vcc, v5, v2
	s_cbranch_vccnz .Lxb1_acq
	s_sleep 1
	s_add_u32 s10, s10, 1
	s_cmp_lt_u32 s10, 0x10000
	s_cbranch_scc1 .Lxb1_spin
	s_branch .Lxb1_acq

.LBB0_3782:
	v_readlane_b32 s4, v254, 43
	s_lshl_b32 s4, s4, 8
	v_readlane_b32 s8, v254, 40
	v_readlane_b32 s9, v254, 41
	s_add_u32 s4, s8, s4
	s_addc_u32 s5, s9, 0
	v_mov_b32_e32 v2, 0x1000
	v_mov_b32_e32 v4, 1
	global_atomic_add v4, v2, v4, s[4:5] offset:1024 sc0
	v_cvt_f32_u32_e32 v2, v3
	v_sub_u32_e32 v5, 0, v3
	v_rcp_iflag_f32_e32 v2, v2
	s_nop 0
	v_mul_f32_e32 v2, 0x4f7ffffe, v2
	v_cvt_u32_f32_e32 v2, v2
	v_mul_lo_u32 v5, v5, v2
	v_mul_hi_u32 v5, v2, v5
	v_add_u32_e32 v2, v2, v5
	s_waitcnt vmcnt(0)
	v_mul_hi_u32 v2, v4, v2
	v_mul_lo_u32 v5, v2, v3
	v_sub_u32_e32 v5, v4, v5
	v_add_u32_e32 v6, 1, v2
	v_cmp_ge_u32_e32 vcc, v5, v3
	v_add_u32_e32 v4, 1, v4
	s_nop 0
	v_cndmask_b32_e32 v2, v2, v6, vcc
	v_sub_u32_e32 v6, v5, v3
	v_cndmask_b32_e32 v5, v5, v6, vcc
	v_add_u32_e32 v6, 1, v2
	v_cmp_ge_u32_e32 vcc, v5, v3
	s_nop 1
	v_cndmask_b32_e32 v2, v2, v6, vcc
	v_mul_lo_u32 v5, v3, v2
	v_add_u32_e32 v3, v5, v3
	v_cmp_ne_u32_e32 vcc, v4, v3
	s_cbranch_vccz .Lxb13_lead
